# nt (streaming) cache policy on the read-once row loads of the two combine passes (layer-1 RP1 and final)
# speedup vs baseline: 1.0034x; 1.0034x over previous
.LBB0_122:
	v_readlane_b32 s8, v253, 40
	v_writelane_b32 v254, s6, 20
	s_xor_b64 s[24:25], s[6:7], -1
	v_readlane_b32 s22, v253, 54
	v_readlane_b32 s23, v253, 55
	s_add_u32 s0, s22, s4
	s_addc_u32 s1, s23, s5
	v_writelane_b32 v254, s7, 21
	s_add_u32 s6, s0, 0x23000000
	v_and_b32_e32 v134, 63, v2
	s_addc_u32 s7, s1, 0
	s_lshl_b32 s26, s28, 3
	v_readlane_b32 s2, v253, 29
	v_writelane_b32 v254, s24, 18
	s_add_i32 s8, s26, s2
	s_lshl_b32 s29, s27, 3
	s_mov_b64 s[2:3], -1
	v_writelane_b32 v254, s25, 19
	s_and_b64 vcc, exec, s[24:25]
	v_lshlrev_b32_e32 v132, 2, v134
	v_readlane_b32 s9, v253, 41
	v_readlane_b32 s10, v253, 42
	v_readlane_b32 s11, v253, 43
	v_readlane_b32 s12, v253, 44
	v_readlane_b32 s13, v253, 45
	v_readlane_b32 s14, v253, 46
	v_readlane_b32 s15, v253, 47
	v_readlane_b32 s16, v253, 48
	v_readlane_b32 s17, v253, 49
	v_readlane_b32 s18, v253, 50
	v_readlane_b32 s19, v253, 51
	v_readlane_b32 s20, v253, 52
	v_readlane_b32 s21, v253, 53
	s_cbranch_vccz .LBB0_164
	v_lshlrev_b32_e32 v22, 3, v134
	s_mov_b32 s2, s8
	s_lshl_b32 s16, s29, 1
	s_add_u32 s10, s0, 0x400000
	s_addc_u32 s11, s1, 0
	s_add_u32 s12, s0, 0x4a000000
	s_addc_u32 s13, s1, 0
	s_add_u32 s14, s0, 0x27000000
	s_addc_u32 s15, s1, 0
	s_cmp_lt_i32 s2, 0x8000
	s_cbranch_scc0 .LBB0_163
	s_lshl_b32 s22, s2, 11
	s_add_u32 s22, s12, s22
	s_addc_u32 s23, s13, 0
	s_lshl_b32 s24, s2, 6
	s_add_u32 s24, s10, s24
	s_addc_u32 s25, s11, 0
	global_load_dwordx2 v[2:3], v22, s[22:23] nt
	global_load_dwordx2 v[4:5], v22, s[22:23] offset:512 nt
	global_load_dwordx2 v[6:7], v22, s[22:23] offset:1024 nt
	global_load_dwordx2 v[8:9], v22, s[22:23] offset:1536 nt
	global_load_dword v18, v132, s[24:25]
	s_add_i32 s31, s2, s29
	s_cmp_lt_i32 s31, 0x8000
	s_cbranch_scc0 .Lrp1_pf_first
	s_lshl_b32 s22, s31, 11
	s_add_u32 s22, s12, s22
	s_addc_u32 s23, s13, 0
	s_lshl_b32 s24, s31, 6
	s_add_u32 s24, s10, s24
	s_addc_u32 s25, s11, 0
	global_load_dwordx2 v[10:11], v22, s[22:23] nt
	global_load_dwordx2 v[12:13], v22, s[22:23] offset:512 nt
	global_load_dwordx2 v[14:15], v22, s[22:23] offset:1024 nt
	global_load_dwordx2 v[16:17], v22, s[22:23] offset:1536 nt
	global_load_dword v19, v132, s[24:25]

.Lrp1_nowait:
	v_lshlrev_b32_e32 v24, 16, v2
	v_and_b32_e32 v25, 0xffff0000, v2
	v_lshlrev_b32_e32 v26, 16, v3
	v_and_b32_e32 v27, 0xffff0000, v3
	v_lshlrev_b32_e32 v28, 16, v4
	v_and_b32_e32 v29, 0xffff0000, v4
	v_lshlrev_b32_e32 v30, 16, v5
	v_and_b32_e32 v31, 0xffff0000, v5
	v_lshlrev_b32_e32 v32, 16, v6
	v_and_b32_e32 v33, 0xffff0000, v6
	v_lshlrev_b32_e32 v34, 16, v7
	v_and_b32_e32 v35, 0xffff0000, v7
	v_lshlrev_b32_e32 v36, 16, v8
	v_and_b32_e32 v37, 0xffff0000, v8
	v_lshlrev_b32_e32 v38, 16, v9
	v_and_b32_e32 v39, 0xffff0000, v9
	v_lshlrev_b32_e32 v40, 16, v10
	v_and_b32_e32 v41, 0xffff0000, v10
	v_lshlrev_b32_e32 v42, 16, v11
	v_and_b32_e32 v43, 0xffff0000, v11
	v_lshlrev_b32_e32 v44, 16, v12
	v_and_b32_e32 v45, 0xffff0000, v12
	v_lshlrev_b32_e32 v46, 16, v13
	v_and_b32_e32 v47, 0xffff0000, v13
	v_lshlrev_b32_e32 v48, 16, v14
	v_and_b32_e32 v49, 0xffff0000, v14
	v_lshlrev_b32_e32 v50, 16, v15
	v_and_b32_e32 v51, 0xffff0000, v15
	v_lshlrev_b32_e32 v52, 16, v16
	v_and_b32_e32 v53, 0xffff0000, v16
	v_lshlrev_b32_e32 v54, 16, v17
	v_and_b32_e32 v55, 0xffff0000, v17
	v_mov_b32_e32 v20, v18
	v_mov_b32_e32 v21, v19
	v_cmp_lt_i32_e32 vcc, -1, v20
	s_and_b32 s19, vcc_lo, 0xffff
	v_cmp_lt_i32_e32 vcc, -1, v21
	s_and_b32 s20, vcc_lo, 0xffff
	s_cmp_eq_u32 s17, 0
	s_cselect_b32 s20, 0, s20
	s_add_i32 s30, s2, s16
	s_cmp_lt_i32 s30, 0x8000
	s_cbranch_scc0 .Lrp1_pf_next
	s_lshl_b32 s22, s30, 11
	s_add_u32 s22, s12, s22
	s_addc_u32 s23, s13, 0
	s_lshl_b32 s24, s30, 6
	s_add_u32 s24, s10, s24
	s_addc_u32 s25, s11, 0
	global_load_dwordx2 v[2:3], v22, s[22:23] nt
	global_load_dwordx2 v[4:5], v22, s[22:23] offset:512 nt
	global_load_dwordx2 v[6:7], v22, s[22:23] offset:1024 nt
	global_load_dwordx2 v[8:9], v22, s[22:23] offset:1536 nt
	global_load_dword v18, v132, s[24:25]
	s_add_i32 s31, s30, s29
	s_cmp_lt_i32 s31, 0x8000
	s_cbranch_scc0 .Lrp1_pf_next
	s_lshl_b32 s22, s31, 11
	s_add_u32 s22, s12, s22
	s_addc_u32 s23, s13, 0
	s_lshl_b32 s24, s31, 6
	s_add_u32 s24, s10, s24
	s_addc_u32 s25, s11, 0
	global_load_dwordx2 v[10:11], v22, s[22:23] nt
	global_load_dwordx2 v[12:13], v22, s[22:23] offset:512 nt
	global_load_dwordx2 v[14:15], v22, s[22:23] offset:1024 nt
	global_load_dwordx2 v[16:17], v22, s[22:23] offset:1536 nt
	global_load_dword v19, v132, s[24:25]

.Lrp1_round:
	s_add_i32 s18, s18, 1
	s_mov_b32 s21, 0
	s_cmp_eq_u32 s19, 0
	s_cbranch_scc1 .Lrp1_iss_A_done
	s_ff1_i32_b32 s0, s19
	s_bitset0_b32 s19, s0
	v_readlane_b32 s1, v20, s0
	s_lshl_b32 s1, s1, 11
	s_add_u32 s22, s14, s1
	s_addc_u32 s23, s15, 0
	global_load_dwordx2 v[56:57], v22, s[22:23] nt
	global_load_dwordx2 v[58:59], v22, s[22:23] offset:512 nt
	global_load_dwordx2 v[60:61], v22, s[22:23] offset:1024 nt
	global_load_dwordx2 v[62:63], v22, s[22:23] offset:1536 nt
	s_bitset1_b32 s21, 0
	s_cmp_eq_u32 s19, 0
	s_cbranch_scc1 .Lrp1_iss_A_done
	s_ff1_i32_b32 s0, s19
	s_bitset0_b32 s19, s0
	v_readlane_b32 s1, v20, s0
	s_lshl_b32 s1, s1, 11
	s_add_u32 s22, s14, s1
	s_addc_u32 s23, s15, 0
	global_load_dwordx2 v[64:65], v22, s[22:23] nt
	global_load_dwordx2 v[66:67], v22, s[22:23] offset:512 nt
	global_load_dwordx2 v[68:69], v22, s[22:23] offset:1024 nt
	global_load_dwordx2 v[70:71], v22, s[22:23] offset:1536 nt
	s_bitset1_b32 s21, 1
	s_cmp_eq_u32 s19, 0
	s_cbranch_scc1 .Lrp1_iss_A_done
	s_ff1_i32_b32 s0, s19
	s_bitset0_b32 s19, s0
	v_readlane_b32 s1, v20, s0
	s_lshl_b32 s1, s1, 11
	s_add_u32 s22, s14, s1
	s_addc_u32 s23, s15, 0
	global_load_dwordx2 v[72:73], v22, s[22:23] nt
	global_load_dwordx2 v[74:75], v22, s[22:23] offset:512 nt
	global_load_dwordx2 v[76:77], v22, s[22:23] offset:1024 nt
	global_load_dwordx2 v[78:79], v22, s[22:23] offset:1536 nt
	s_bitset1_b32 s21, 2
.Lrp1_iss_A_done:
	s_cmp_eq_u32 s20, 0
	s_cbranch_scc1 .Lrp1_iss_B_done
	s_ff1_i32_b32 s0, s20
	s_bitset0_b32 s20, s0
	v_readlane_b32 s1, v21, s0
	s_lshl_b32 s1, s1, 11
	s_add_u32 s22, s14, s1
	s_addc_u32 s23, s15, 0
	global_load_dwordx2 v[80:81], v22, s[22:23] nt
	global_load_dwordx2 v[82:83], v22, s[22:23] offset:512 nt
	global_load_dwordx2 v[84:85], v22, s[22:23] offset:1024 nt
	global_load_dwordx2 v[86:87], v22, s[22:23] offset:1536 nt
	s_bitset1_b32 s21, 3
	s_cmp_eq_u32 s20, 0
	s_cbranch_scc1 .Lrp1_iss_B_done
	s_ff1_i32_b32 s0, s20
	s_bitset0_b32 s20, s0
	v_readlane_b32 s1, v21, s0
	s_lshl_b32 s1, s1, 11
	s_add_u32 s22, s14, s1
	s_addc_u32 s23, s15, 0
	global_load_dwordx2 v[88:89], v22, s[22:23] nt
	global_load_dwordx2 v[90:91], v22, s[22:23] offset:512 nt
	global_load_dwordx2 v[92:93], v22, s[22:23] offset:1024 nt
	global_load_dwordx2 v[94:95], v22, s[22:23] offset:1536 nt
	s_bitset1_b32 s21, 4
	s_cmp_eq_u32 s20, 0
	s_cbranch_scc1 .Lrp1_iss_B_done
	s_ff1_i32_b32 s0, s20
	s_bitset0_b32 s20, s0
	v_readlane_b32 s1, v21, s0
	s_lshl_b32 s1, s1, 11
	s_add_u32 s22, s14, s1
	s_addc_u32 s23, s15, 0
	global_load_dwordx2 v[96:97], v22, s[22:23] nt
	global_load_dwordx2 v[98:99], v22, s[22:23] offset:512 nt
	global_load_dwordx2 v[100:101], v22, s[22:23] offset:1024 nt
	global_load_dwordx2 v[102:103], v22, s[22:23] offset:1536 nt
	s_bitset1_b32 s21, 5

.LBB0_1110:
	v_readlane_b32 s26, v253, 54
	v_readlane_b32 s27, v253, 55
	v_readlane_b32 s1, v253, 29
	v_readlane_b32 s22, v253, 50
	v_readlane_b32 s23, v253, 51
	v_readlane_b32 s24, v253, 52
	v_readlane_b32 s25, v253, 53
	v_and_b32_e32 v104, 63, v0
	v_lshlrev_b32_e32 v105, 3, v104
	v_lshlrev_b32_e32 v106, 2, v104
	v_lshlrev_b32_e32 v107, 4, v104
	v_mov_b32_e32 v108, 0x358637bd
	v_mov_b32_e32 v109, 0x260
	s_mov_b32 s35, 0xf800000
	s_lshl_b32 s0, s5, 3
	s_add_i32 s2, s0, s1
	s_lshl_b32 s20, s37, 3
	s_lshl_b32 s21, s37, 4
	s_add_u32 s4, s26, 0x400000
	s_addc_u32 s5, s27, 0
	s_add_u32 s6, s26, 0x4a000000
	s_addc_u32 s7, s27, 0
	s_add_u32 s8, s26, 0x27000000
	s_addc_u32 s9, s27, 0
	s_cmp_lt_i32 s2, 0x8000
	s_cbranch_scc0 .LBB0_1150
	global_load_dwordx4 v[112:115], v107, s[22:23]
	global_load_dwordx4 v[116:119], v107, s[22:23] offset:1024
	global_load_dwordx4 v[120:123], v107, s[22:23] offset:2048
	global_load_dwordx4 v[124:127], v107, s[22:23] offset:3072
	s_lshl_b32 s10, s2, 11
	s_add_u32 s10, s6, s10
	s_addc_u32 s11, s7, 0
	s_lshl_b32 s12, s2, 6
	s_add_u32 s12, s4, s12
	s_addc_u32 s13, s5, 0
	global_load_dwordx2 v[0:1], v105, s[10:11] nt
	global_load_dwordx2 v[2:3], v105, s[10:11] offset:512 nt
	global_load_dwordx2 v[4:5], v105, s[10:11] offset:1024 nt
	global_load_dwordx2 v[6:7], v105, s[10:11] offset:1536 nt
	global_load_dword v16, v106, s[12:13]
	s_add_i32 s34, s2, s20
	s_cmp_lt_i32 s34, 0x8000
	s_cbranch_scc0 .Lfin_pf_first
	s_lshl_b32 s10, s34, 11
	s_add_u32 s10, s6, s10
	s_addc_u32 s11, s7, 0
	s_lshl_b32 s12, s34, 6
	s_add_u32 s12, s4, s12
	s_addc_u32 s13, s5, 0
	global_load_dwordx2 v[8:9], v105, s[10:11] nt
	global_load_dwordx2 v[10:11], v105, s[10:11] offset:512 nt
	global_load_dwordx2 v[12:13], v105, s[10:11] offset:1024 nt
	global_load_dwordx2 v[14:15], v105, s[10:11] offset:1536 nt
	global_load_dword v17, v106, s[12:13]

.Lfin_nowait:
	v_lshlrev_b32_e32 v32, 16, v0
	v_and_b32_e32 v33, 0xffff0000, v0
	v_lshlrev_b32_e32 v34, 16, v1
	v_and_b32_e32 v35, 0xffff0000, v1
	v_lshlrev_b32_e32 v36, 16, v2
	v_and_b32_e32 v37, 0xffff0000, v2
	v_lshlrev_b32_e32 v38, 16, v3
	v_and_b32_e32 v39, 0xffff0000, v3
	v_lshlrev_b32_e32 v40, 16, v4
	v_and_b32_e32 v41, 0xffff0000, v4
	v_lshlrev_b32_e32 v42, 16, v5
	v_and_b32_e32 v43, 0xffff0000, v5
	v_lshlrev_b32_e32 v44, 16, v6
	v_and_b32_e32 v45, 0xffff0000, v6
	v_lshlrev_b32_e32 v46, 16, v7
	v_and_b32_e32 v47, 0xffff0000, v7
	v_lshlrev_b32_e32 v48, 16, v8
	v_and_b32_e32 v49, 0xffff0000, v8
	v_lshlrev_b32_e32 v50, 16, v9
	v_and_b32_e32 v51, 0xffff0000, v9
	v_lshlrev_b32_e32 v52, 16, v10
	v_and_b32_e32 v53, 0xffff0000, v10
	v_lshlrev_b32_e32 v54, 16, v11
	v_and_b32_e32 v55, 0xffff0000, v11
	v_lshlrev_b32_e32 v56, 16, v12
	v_and_b32_e32 v57, 0xffff0000, v12
	v_lshlrev_b32_e32 v58, 16, v13
	v_and_b32_e32 v59, 0xffff0000, v13
	v_lshlrev_b32_e32 v60, 16, v14
	v_and_b32_e32 v61, 0xffff0000, v14
	v_lshlrev_b32_e32 v62, 16, v15
	v_and_b32_e32 v63, 0xffff0000, v15
	v_mov_b32_e32 v18, v16
	v_mov_b32_e32 v19, v17
	v_cmp_lt_i32_e32 vcc, -1, v18
	s_and_b32 s30, vcc_lo, 0xffff
	v_cmp_lt_i32_e32 vcc, -1, v19
	s_and_b32 s31, vcc_lo, 0xffff
	s_cmp_eq_u32 s29, 0
	s_cselect_b32 s31, 0, s31
	s_add_i32 s33, s2, s21
	s_cmp_lt_i32 s33, 0x8000
	s_cbranch_scc0 .Lfin_pf_next
	s_lshl_b32 s10, s33, 11
	s_add_u32 s10, s6, s10
	s_addc_u32 s11, s7, 0
	s_lshl_b32 s12, s33, 6
	s_add_u32 s12, s4, s12
	s_addc_u32 s13, s5, 0
	global_load_dwordx2 v[0:1], v105, s[10:11] nt
	global_load_dwordx2 v[2:3], v105, s[10:11] offset:512 nt
	global_load_dwordx2 v[4:5], v105, s[10:11] offset:1024 nt
	global_load_dwordx2 v[6:7], v105, s[10:11] offset:1536 nt
	global_load_dword v16, v106, s[12:13]
	s_add_i32 s34, s33, s20
	s_cmp_lt_i32 s34, 0x8000
	s_cbranch_scc0 .Lfin_pf_next
	s_lshl_b32 s10, s34, 11
	s_add_u32 s10, s6, s10
	s_addc_u32 s11, s7, 0
	s_lshl_b32 s12, s34, 6
	s_add_u32 s12, s4, s12
	s_addc_u32 s13, s5, 0
	global_load_dwordx2 v[8:9], v105, s[10:11] nt
	global_load_dwordx2 v[10:11], v105, s[10:11] offset:512 nt
	global_load_dwordx2 v[12:13], v105, s[10:11] offset:1024 nt
	global_load_dwordx2 v[14:15], v105, s[10:11] offset:1536 nt
	global_load_dword v17, v106, s[12:13]

.Lfin_round:
	s_add_i32 s28, s28, 1
	s_mov_b32 s36, 0
	s_cmp_eq_u32 s30, 0
	s_cbranch_scc1 .Lfin_iss_A_done
	s_ff1_i32_b32 s14, s30
	s_bitset0_b32 s30, s14
	v_readlane_b32 s15, v18, s14
	s_lshl_b32 s15, s15, 11
	s_add_u32 s16, s8, s15
	s_addc_u32 s17, s9, 0
	global_load_dwordx2 v[128:129], v105, s[16:17] nt
	global_load_dwordx2 v[130:131], v105, s[16:17] offset:512 nt
	global_load_dwordx2 v[132:133], v105, s[16:17] offset:1024 nt
	global_load_dwordx2 v[134:135], v105, s[16:17] offset:1536 nt
	s_bitset1_b32 s36, 0
	s_cmp_eq_u32 s30, 0
	s_cbranch_scc1 .Lfin_iss_A_done
	s_ff1_i32_b32 s14, s30
	s_bitset0_b32 s30, s14
	v_readlane_b32 s15, v18, s14
	s_lshl_b32 s15, s15, 11
	s_add_u32 s16, s8, s15
	s_addc_u32 s17, s9, 0
	global_load_dwordx2 v[136:137], v105, s[16:17] nt
	global_load_dwordx2 v[138:139], v105, s[16:17] offset:512 nt
	global_load_dwordx2 v[140:141], v105, s[16:17] offset:1024 nt
	global_load_dwordx2 v[142:143], v105, s[16:17] offset:1536 nt
	s_bitset1_b32 s36, 1
	s_cmp_eq_u32 s30, 0
	s_cbranch_scc1 .Lfin_iss_A_done
	s_ff1_i32_b32 s14, s30
	s_bitset0_b32 s30, s14
	v_readlane_b32 s15, v18, s14
	s_lshl_b32 s15, s15, 11
	s_add_u32 s16, s8, s15
	s_addc_u32 s17, s9, 0
	global_load_dwordx2 v[144:145], v105, s[16:17] nt
	global_load_dwordx2 v[146:147], v105, s[16:17] offset:512 nt
	global_load_dwordx2 v[148:149], v105, s[16:17] offset:1024 nt
	global_load_dwordx2 v[150:151], v105, s[16:17] offset:1536 nt
	s_bitset1_b32 s36, 2
	s_cmp_eq_u32 s30, 0
	s_cbranch_scc1 .Lfin_iss_A_done
	s_ff1_i32_b32 s14, s30
	s_bitset0_b32 s30, s14
	v_readlane_b32 s15, v18, s14
	s_lshl_b32 s15, s15, 11
	s_add_u32 s16, s8, s15
	s_addc_u32 s17, s9, 0
	global_load_dwordx2 v[152:153], v105, s[16:17] nt
	global_load_dwordx2 v[154:155], v105, s[16:17] offset:512 nt
	global_load_dwordx2 v[156:157], v105, s[16:17] offset:1024 nt
	global_load_dwordx2 v[158:159], v105, s[16:17] offset:1536 nt
	s_bitset1_b32 s36, 3
.Lfin_iss_A_done:
	s_cmp_eq_u32 s31, 0
	s_cbranch_scc1 .Lfin_iss_B_done
	s_ff1_i32_b32 s14, s31
	s_bitset0_b32 s31, s14
	v_readlane_b32 s15, v19, s14
	s_lshl_b32 s15, s15, 11
	s_add_u32 s16, s8, s15
	s_addc_u32 s17, s9, 0
	global_load_dwordx2 v[160:161], v105, s[16:17] nt
	global_load_dwordx2 v[162:163], v105, s[16:17] offset:512 nt
	global_load_dwordx2 v[164:165], v105, s[16:17] offset:1024 nt
	global_load_dwordx2 v[166:167], v105, s[16:17] offset:1536 nt
	s_bitset1_b32 s36, 4
	s_cmp_eq_u32 s31, 0
	s_cbranch_scc1 .Lfin_iss_B_done
	s_ff1_i32_b32 s14, s31
	s_bitset0_b32 s31, s14
	v_readlane_b32 s15, v19, s14
	s_lshl_b32 s15, s15, 11
	s_add_u32 s16, s8, s15
	s_addc_u32 s17, s9, 0
	global_load_dwordx2 v[168:169], v105, s[16:17] nt
	global_load_dwordx2 v[170:171], v105, s[16:17] offset:512 nt
	global_load_dwordx2 v[172:173], v105, s[16:17] offset:1024 nt
	global_load_dwordx2 v[174:175], v105, s[16:17] offset:1536 nt
	s_bitset1_b32 s36, 5
	s_cmp_eq_u32 s31, 0
	s_cbranch_scc1 .Lfin_iss_B_done
	s_ff1_i32_b32 s14, s31
	s_bitset0_b32 s31, s14
	v_readlane_b32 s15, v19, s14
	s_lshl_b32 s15, s15, 11
	s_add_u32 s16, s8, s15
	s_addc_u32 s17, s9, 0
	global_load_dwordx2 v[176:177], v105, s[16:17] nt
	global_load_dwordx2 v[178:179], v105, s[16:17] offset:512 nt
	global_load_dwordx2 v[180:181], v105, s[16:17] offset:1024 nt
	global_load_dwordx2 v[182:183], v105, s[16:17] offset:1536 nt
	s_bitset1_b32 s36, 6
	s_cmp_eq_u32 s31, 0
	s_cbranch_scc1 .Lfin_iss_B_done
	s_ff1_i32_b32 s14, s31
	s_bitset0_b32 s31, s14
	v_readlane_b32 s15, v19, s14
	s_lshl_b32 s15, s15, 11
	s_add_u32 s16, s8, s15
	s_addc_u32 s17, s9, 0
	global_load_dwordx2 v[184:185], v105, s[16:17] nt
	global_load_dwordx2 v[186:187], v105, s[16:17] offset:512 nt
	global_load_dwordx2 v[188:189], v105, s[16:17] offset:1024 nt
	global_load_dwordx2 v[190:191], v105, s[16:17] offset:1536 nt
	s_bitset1_b32 s36, 7
